# v24 + s_setprio 1 during the QK/softmax section and 0 during P.V in both diff-attention loops
# speedup vs baseline: 1.0142x; 1.0142x over previous
.LBB0_188:
	s_setprio 0
	s_waitcnt lgkmcnt(0)
	v_add_u32_e32 v0, s44, v224
	ds_read_b64_tr_b16 v[160:161], v0 offset:0
	ds_read_b64_tr_b16 v[162:163], v0 offset:0x800
	ds_read_b64_tr_b16 v[164:165], v0 offset:0x200
	ds_read_b64_tr_b16 v[166:167], v0 offset:0xa00
	ds_read_b64_tr_b16 v[168:169], v0 offset:0x400
	ds_read_b64_tr_b16 v[170:171], v0 offset:0xc00
	ds_read_b64_tr_b16 v[172:173], v0 offset:0x600
	ds_read_b64_tr_b16 v[174:175], v0 offset:0xe00
	s_waitcnt lgkmcnt(4)
	s_nop 0
	v_mfma_f32_32x32x16_bf16 v[112:127], v[208:211], v[160:163], v[112:127]
	v_mfma_f32_32x32x16_bf16 v[96:111], v[208:211], v[164:167], v[96:111]
	v_mfma_f32_32x32x16_bf16 v[128:143], v[156:159], v[160:163], v[128:143]
	v_mfma_f32_32x32x16_bf16 v[80:95], v[156:159], v[164:167], v[80:95]
	ds_read_b64_tr_b16 v[160:161], v0 offset:0x1000
	ds_read_b64_tr_b16 v[162:163], v0 offset:0x1800
	ds_read_b64_tr_b16 v[164:165], v0 offset:0x1200
	ds_read_b64_tr_b16 v[166:167], v0 offset:0x1a00
	s_waitcnt lgkmcnt(4)
	v_mfma_f32_32x32x16_bf16 v[64:79], v[208:211], v[168:171], v[64:79]
	v_mfma_f32_32x32x16_bf16 v[48:63], v[208:211], v[172:175], v[48:63]
	v_mfma_f32_32x32x16_bf16 v[32:47], v[156:159], v[168:171], v[32:47]
	v_mfma_f32_32x32x16_bf16 v[16:31], v[156:159], v[172:175], v[16:31]
	ds_read_b64_tr_b16 v[156:157], v0 offset:0x1400
	ds_read_b64_tr_b16 v[158:159], v0 offset:0x1c00
	ds_read_b64_tr_b16 v[168:169], v0 offset:0x1600
	ds_read_b64_tr_b16 v[170:171], v0 offset:0x1e00
	s_waitcnt lgkmcnt(4)
	v_mfma_f32_32x32x16_bf16 v[112:127], v[10:13], v[160:163], v[112:127]
	v_mfma_f32_32x32x16_bf16 v[96:111], v[10:13], v[164:167], v[96:111]
	v_mfma_f32_32x32x16_bf16 v[128:143], v[152:155], v[160:163], v[128:143]
	v_mfma_f32_32x32x16_bf16 v[80:95], v[152:155], v[164:167], v[80:95]
	ds_read_b64_tr_b16 v[160:161], v0 offset:0x2000
	ds_read_b64_tr_b16 v[162:163], v0 offset:0x2800
	ds_read_b64_tr_b16 v[164:165], v0 offset:0x2200
	ds_read_b64_tr_b16 v[166:167], v0 offset:0x2a00
	s_waitcnt lgkmcnt(4)
	v_mfma_f32_32x32x16_bf16 v[64:79], v[10:13], v[156:159], v[64:79]
	v_mfma_f32_32x32x16_bf16 v[48:63], v[10:13], v[168:171], v[48:63]
	v_mfma_f32_32x32x16_bf16 v[32:47], v[152:155], v[156:159], v[32:47]
	v_mfma_f32_32x32x16_bf16 v[16:31], v[152:155], v[168:171], v[16:31]
	ds_read_b64_tr_b16 v[10:11], v0 offset:0x2400
	ds_read_b64_tr_b16 v[12:13], v0 offset:0x2c00
	ds_read_b64_tr_b16 v[152:153], v0 offset:0x2600
	ds_read_b64_tr_b16 v[154:155], v0 offset:0x2e00
	s_waitcnt lgkmcnt(4)
	v_mfma_f32_32x32x16_bf16 v[112:127], v[6:9], v[160:163], v[112:127]
	v_mfma_f32_32x32x16_bf16 v[96:111], v[6:9], v[164:167], v[96:111]
	v_mfma_f32_32x32x16_bf16 v[128:143], v[148:151], v[160:163], v[128:143]
	v_mfma_f32_32x32x16_bf16 v[80:95], v[148:151], v[164:167], v[80:95]
	ds_read_b64_tr_b16 v[156:157], v0 offset:0x3000
	ds_read_b64_tr_b16 v[158:159], v0 offset:0x3800
	ds_read_b64_tr_b16 v[160:161], v0 offset:0x3200
	ds_read_b64_tr_b16 v[162:163], v0 offset:0x3a00
	s_waitcnt lgkmcnt(4)
	v_mfma_f32_32x32x16_bf16 v[64:79], v[6:9], v[10:13], v[64:79]
	v_mfma_f32_32x32x16_bf16 v[48:63], v[6:9], v[152:155], v[48:63]
	v_mfma_f32_32x32x16_bf16 v[32:47], v[148:151], v[10:13], v[32:47]
	v_mfma_f32_32x32x16_bf16 v[16:31], v[148:151], v[152:155], v[16:31]
	ds_read_b64_tr_b16 v[6:7], v0 offset:0x3400
	ds_read_b64_tr_b16 v[8:9], v0 offset:0x3c00
	ds_read_b64_tr_b16 v[10:11], v0 offset:0x3600
	ds_read_b64_tr_b16 v[12:13], v0 offset:0x3e00
	s_waitcnt lgkmcnt(4)
	v_mfma_f32_32x32x16_bf16 v[112:127], v[2:5], v[156:159], v[112:127]
	v_mfma_f32_32x32x16_bf16 v[96:111], v[2:5], v[160:163], v[96:111]
	v_mfma_f32_32x32x16_bf16 v[128:143], v[144:147], v[156:159], v[128:143]
	v_mfma_f32_32x32x16_bf16 v[80:95], v[144:147], v[160:163], v[80:95]
	s_waitcnt lgkmcnt(0)
	v_mfma_f32_32x32x16_bf16 v[64:79], v[2:5], v[6:9], v[64:79]
	v_mfma_f32_32x32x16_bf16 v[48:63], v[2:5], v[10:13], v[48:63]
	v_mfma_f32_32x32x16_bf16 v[32:47], v[144:147], v[6:9], v[32:47]
	v_mfma_f32_32x32x16_bf16 v[16:31], v[144:147], v[10:13], v[16:31]
.LBB0_189:
	s_setprio 1
	s_add_i32 s44, s73, 0xfffffdb2
	s_cmp_gt_u32 s44, 0xfffffb44
	s_cselect_b64 s[42:43], -1, 0
	s_cmp_lt_u32 s44, 0xfffffb45
	s_cselect_b64 vcc, -1, 0
	s_cmp_gt_i32 s73, -1
	s_cselect_b64 s[44:45], -1, 0
	s_xor_b64 s[44:45], s[0:1], s[44:45]
	v_add_u32_e32 v212, s71, v243
	s_and_b64 s[44:45], vcc, s[44:45]
	v_add_u32_e32 v213, 0x21700, v212
	s_and_b64 vcc, exec, vcc
	s_cbranch_vccnz .LBB0_194
	v_add_u32_e32 v0, 0x21780, v212
	v_add_u32_e32 v2, 0x21708, v212
	v_add_u32_e32 v3, 0x21788, v212
	ds_read2_b32 v[144:145], v213 offset1:1
	ds_read2_b32 v[160:161], v0 offset1:1
	ds_read2_b32 v[146:147], v2 offset1:1
	ds_read2_b32 v[162:163], v3 offset1:1
	v_add_u32_e32 v0, 0x21720, v212
	v_add_u32_e32 v2, 0x217a0, v212
	v_add_u32_e32 v3, 0x21728, v212
	v_add_u32_e32 v4, 0x217a8, v212
	ds_read2_b32 v[148:149], v0 offset1:1
	ds_read2_b32 v[164:165], v2 offset1:1
	ds_read2_b32 v[150:151], v3 offset1:1
	ds_read2_b32 v[166:167], v4 offset1:1
	v_add_u32_e32 v0, 0x21740, v212
	v_add_u32_e32 v2, 0x217c0, v212
	v_add_u32_e32 v3, 0x21748, v212
	v_add_u32_e32 v4, 0x217c8, v212
	ds_read2_b32 v[152:153], v0 offset1:1
	ds_read2_b32 v[168:169], v2 offset1:1
	ds_read2_b32 v[154:155], v3 offset1:1
	ds_read2_b32 v[170:171], v4 offset1:1
	v_add_u32_e32 v0, 0x21760, v212
	v_add_u32_e32 v2, 0x217e0, v212
	v_add_u32_e32 v3, 0x21768, v212
	v_add_u32_e32 v4, 0x217e8, v212
	ds_read2_b32 v[156:157], v0 offset1:1
	ds_read2_b32 v[172:173], v2 offset1:1
	ds_read2_b32 v[158:159], v3 offset1:1
	ds_read2_b32 v[174:175], v4 offset1:1
	s_branch .LBB0_195

.LBB0_205:
	v_add_u32_e32 v219, v212, v232
	v_add_u32_e32 v212, v212, v233
	s_waitcnt lgkmcnt(0)
	v_mfma_f32_32x32x16_bf16 v[144:159], v[248:251], v[192:195], v[144:159]
	ds_read_b128 v[248:251], v219
	v_mfma_f32_32x32x16_bf16 v[160:175], v[236:239], v[192:195], v[160:175]
	ds_read_b128 v[236:239], v219 offset:8192
	v_mfma_f32_32x32x16_bf16 v[144:159], v[240:243], v[196:199], v[144:159]
	ds_read_b128 v[240:243], v212
	v_mfma_f32_32x32x16_bf16 v[160:175], v[244:247], v[196:199], v[160:175]
	ds_read_b128 v[244:247], v212 offset:8192
	s_waitcnt lgkmcnt(3)
	v_mfma_f32_32x32x16_bf16 v[144:159], v[248:251], v[200:203], v[144:159]
	s_waitcnt lgkmcnt(2)
	v_mfma_f32_32x32x16_bf16 v[160:175], v[236:239], v[200:203], v[160:175]
	v_add_f32_e32 v212, v213, v218
	v_add_f32_e32 v235, v235, v212
	s_waitcnt lgkmcnt(1)
	v_mfma_f32_32x32x16_bf16 v[144:159], v[240:243], v[204:207], v[144:159]
	s_waitcnt lgkmcnt(0)
	v_mfma_f32_32x32x16_bf16 v[160:175], v[244:247], v[204:207], v[160:175]
	s_nop 10
	v_exp_f32_e32 v212, v144
	v_exp_f32_e32 v218, v145
	v_exp_f32_e32 v242, v148
	v_exp_f32_e32 v244, v149
	v_exp_f32_e32 v213, v152
	v_exp_f32_e32 v219, v153
	v_exp_f32_e32 v243, v156
	v_exp_f32_e32 v245, v157
	v_exp_f32_e32 v236, v146
	v_exp_f32_e32 v150, v150
	v_exp_f32_e32 v248, v151
	v_exp_f32_e32 v237, v154
	v_exp_f32_e32 v151, v158
	v_exp_f32_e32 v238, v147
	v_exp_f32_e32 v239, v155
	v_exp_f32_e32 v249, v159
	v_exp_f32_e32 v160, v160
	v_exp_f32_e32 v220, v161
	v_exp_f32_e32 v164, v164
	v_exp_f32_e32 v246, v165
	v_exp_f32_e32 v161, v168
	v_exp_f32_e32 v165, v172
	v_exp_f32_e32 v221, v169
	v_exp_f32_e32 v247, v173
	v_pk_add_f32 v[144:145], v[212:213], v[218:219]
	v_pk_add_f32 v[146:147], v[242:243], v[244:245]
	v_exp_f32_e32 v162, v162
	v_exp_f32_e32 v240, v163
	v_exp_f32_e32 v166, v166
	v_exp_f32_e32 v250, v167
	v_exp_f32_e32 v163, v170
	v_exp_f32_e32 v167, v174
	v_pk_add_f32 v[144:145], v[236:237], v[144:145]
	v_pk_add_f32 v[146:147], v[150:151], v[146:147]
	v_exp_f32_e32 v241, v171
	v_exp_f32_e32 v251, v175
	v_pk_add_f32 v[144:145], v[238:239], v[144:145]
	v_pk_add_f32 v[146:147], v[248:249], v[146:147]
	v_pk_add_f32 v[144:145], v[160:161], v[144:145]
	v_pk_add_f32 v[146:147], v[164:165], v[146:147]
	v_pk_add_f32 v[144:145], v[220:221], v[144:145]
	v_pk_add_f32 v[146:147], v[246:247], v[146:147]
	v_pk_add_f32 v[144:145], v[162:163], v[144:145]
	v_pk_add_f32 v[146:147], v[166:167], v[146:147]
	v_pk_add_f32 v[144:145], v[240:241], v[144:145]
	v_pk_add_f32 v[146:147], v[250:251], v[146:147]
	v_cvt_pk_bf16_f32 v148, v213, v219
	v_pk_add_f32 v[144:145], v[144:145], v[146:147]
	v_cvt_pk_bf16_f32 v146, v242, v244
	v_pk_add_f32 v[144:145], v[144:145], v[144:145] op_sel:[0,1] op_sel_hi:[1,0]
	v_cvt_pk_bf16_f32 v147, v150, v248
	v_mov_b32_e32 v145, v144
	s_nop 1
	v_permlane32_swap_b32_e32 v144, v145
	v_add_f32_e32 v144, v144, v145
	v_add_f32_e32 v234, v234, v144
	v_cvt_pk_bf16_f32 v144, v212, v218
	v_cvt_pk_bf16_f32 v145, v236, v238
	v_cvt_pk_bf16_f32 v149, v237, v239
	v_cvt_pk_bf16_f32 v150, v243, v245
	v_cvt_pk_bf16_f32 v151, v151, v249
	v_cvt_pk_bf16_f32 v152, v160, v220
	v_cvt_pk_bf16_f32 v153, v162, v240
	v_cvt_pk_bf16_f32 v154, v164, v246
	v_cvt_pk_bf16_f32 v155, v166, v250
	v_cvt_pk_bf16_f32 v156, v161, v221
	v_cvt_pk_bf16_f32 v157, v163, v241
	v_cvt_pk_bf16_f32 v158, v165, v247
	v_cvt_pk_bf16_f32 v159, v167, v251
	v_permlane32_swap_b32_e32 v144, v146
	v_permlane32_swap_b32_e32 v145, v147
	v_permlane32_swap_b32_e32 v148, v150
	v_permlane32_swap_b32_e32 v149, v151
	v_permlane32_swap_b32_e32 v152, v154
	v_permlane32_swap_b32_e32 v153, v155
	v_permlane32_swap_b32_e32 v156, v158
	v_permlane32_swap_b32_e32 v157, v159
	s_setprio 0
	s_waitcnt lgkmcnt(0)
	v_add_u32_e32 v212, s56, v224
	ds_read_b64_tr_b16 v[160:161], v212 offset:0
	ds_read_b64_tr_b16 v[162:163], v212 offset:0x800
	ds_read_b64_tr_b16 v[164:165], v212 offset:0x200
	ds_read_b64_tr_b16 v[166:167], v212 offset:0xa00
	ds_read_b64_tr_b16 v[168:169], v212 offset:0x400
	ds_read_b64_tr_b16 v[170:171], v212 offset:0xc00
	ds_read_b64_tr_b16 v[172:173], v212 offset:0x600
	ds_read_b64_tr_b16 v[174:175], v212 offset:0xe00
	s_waitcnt lgkmcnt(4)
	s_nop 0
	v_mfma_f32_32x32x16_bf16 v[112:127], v[208:211], v[160:163], v[112:127]
	v_mfma_f32_32x32x16_bf16 v[96:111], v[208:211], v[164:167], v[96:111]
	v_mfma_f32_32x32x16_bf16 v[128:143], v[144:147], v[160:163], v[128:143]
	v_mfma_f32_32x32x16_bf16 v[80:95], v[144:147], v[164:167], v[80:95]
	ds_read_b64_tr_b16 v[160:161], v212 offset:0x1000
	ds_read_b64_tr_b16 v[162:163], v212 offset:0x1800
	ds_read_b64_tr_b16 v[164:165], v212 offset:0x1200
	ds_read_b64_tr_b16 v[166:167], v212 offset:0x1a00
	s_waitcnt lgkmcnt(4)
	v_mfma_f32_32x32x16_bf16 v[64:79], v[208:211], v[168:171], v[64:79]
	v_mfma_f32_32x32x16_bf16 v[48:63], v[208:211], v[172:175], v[48:63]
	v_mfma_f32_32x32x16_bf16 v[32:47], v[144:147], v[168:171], v[32:47]
	v_mfma_f32_32x32x16_bf16 v[16:31], v[144:147], v[172:175], v[16:31]
	ds_read_b64_tr_b16 v[144:145], v212 offset:0x1400
	ds_read_b64_tr_b16 v[146:147], v212 offset:0x1c00
	ds_read_b64_tr_b16 v[168:169], v212 offset:0x1600
	ds_read_b64_tr_b16 v[170:171], v212 offset:0x1e00
	s_waitcnt lgkmcnt(4)
	v_mfma_f32_32x32x16_bf16 v[112:127], v[10:13], v[160:163], v[112:127]
	v_mfma_f32_32x32x16_bf16 v[96:111], v[10:13], v[164:167], v[96:111]
	v_mfma_f32_32x32x16_bf16 v[128:143], v[148:151], v[160:163], v[128:143]
	v_mfma_f32_32x32x16_bf16 v[80:95], v[148:151], v[164:167], v[80:95]
	ds_read_b64_tr_b16 v[160:161], v212 offset:0x2000
	ds_read_b64_tr_b16 v[162:163], v212 offset:0x2800
	ds_read_b64_tr_b16 v[164:165], v212 offset:0x2200
	ds_read_b64_tr_b16 v[166:167], v212 offset:0x2a00
	s_waitcnt lgkmcnt(4)
	v_mfma_f32_32x32x16_bf16 v[64:79], v[10:13], v[144:147], v[64:79]
	v_mfma_f32_32x32x16_bf16 v[48:63], v[10:13], v[168:171], v[48:63]
	v_mfma_f32_32x32x16_bf16 v[32:47], v[148:151], v[144:147], v[32:47]
	v_mfma_f32_32x32x16_bf16 v[16:31], v[148:151], v[168:171], v[16:31]
	ds_read_b64_tr_b16 v[10:11], v212 offset:0x2400
	ds_read_b64_tr_b16 v[12:13], v212 offset:0x2c00
	ds_read_b64_tr_b16 v[144:145], v212 offset:0x2600
	ds_read_b64_tr_b16 v[146:147], v212 offset:0x2e00
	s_waitcnt lgkmcnt(4)
	v_mfma_f32_32x32x16_bf16 v[112:127], v[6:9], v[160:163], v[112:127]
	v_mfma_f32_32x32x16_bf16 v[96:111], v[6:9], v[164:167], v[96:111]
	v_mfma_f32_32x32x16_bf16 v[128:143], v[152:155], v[160:163], v[128:143]
	v_mfma_f32_32x32x16_bf16 v[80:95], v[152:155], v[164:167], v[80:95]
	ds_read_b64_tr_b16 v[148:149], v212 offset:0x3000
	ds_read_b64_tr_b16 v[150:151], v212 offset:0x3800
	ds_read_b64_tr_b16 v[160:161], v212 offset:0x3200
	ds_read_b64_tr_b16 v[162:163], v212 offset:0x3a00
	s_waitcnt lgkmcnt(4)
	v_mfma_f32_32x32x16_bf16 v[64:79], v[6:9], v[10:13], v[64:79]
	v_mfma_f32_32x32x16_bf16 v[48:63], v[6:9], v[144:147], v[48:63]
	v_mfma_f32_32x32x16_bf16 v[32:47], v[152:155], v[10:13], v[32:47]
	v_mfma_f32_32x32x16_bf16 v[16:31], v[152:155], v[144:147], v[16:31]
	ds_read_b64_tr_b16 v[6:7], v212 offset:0x3400
	ds_read_b64_tr_b16 v[8:9], v212 offset:0x3c00
	ds_read_b64_tr_b16 v[10:11], v212 offset:0x3600
	ds_read_b64_tr_b16 v[12:13], v212 offset:0x3e00
	s_waitcnt lgkmcnt(4)
	v_mfma_f32_32x32x16_bf16 v[112:127], v[2:5], v[148:151], v[112:127]
	v_mfma_f32_32x32x16_bf16 v[96:111], v[2:5], v[160:163], v[96:111]
	v_mfma_f32_32x32x16_bf16 v[128:143], v[156:159], v[148:151], v[128:143]
	v_mfma_f32_32x32x16_bf16 v[80:95], v[156:159], v[160:163], v[80:95]
	s_waitcnt lgkmcnt(0)
	v_mfma_f32_32x32x16_bf16 v[64:79], v[2:5], v[6:9], v[64:79]
	v_mfma_f32_32x32x16_bf16 v[48:63], v[2:5], v[10:13], v[48:63]
	v_mfma_f32_32x32x16_bf16 v[32:47], v[156:159], v[6:9], v[32:47]
	v_mfma_f32_32x32x16_bf16 v[16:31], v[156:159], v[10:13], v[16:31]
	s_add_i32 s42, s56, 0x4000
	s_cmpk_lg_u32 s56, 0xc000
	s_cselect_b32 s56, s42, 0
	s_add_i32 s42, s90, 0x4000
	s_cmpk_lg_u32 s90, 0xc000
	s_cselect_b32 s90, s42, 0
	s_add_u32 s40, s40, 0x60000
	s_addc_u32 s41, s41, 0
	s_addk_i32 s73, 0x100
	s_add_i32 s72, s72, 64
	s_add_i32 s71, s71, 1
	s_cmpk_eq_i32 s73, 0x4000
	s_cbranch_scc1 .LBB0_220

.LBB0_210:
	s_setprio 1
	s_add_i32 s44, s72, 0xfffffdb2
	s_cmp_gt_u32 s44, 0xfffffb44
	s_cselect_b64 s[42:43], -1, 0
	s_cmp_lt_u32 s44, 0xfffffb45
	s_cselect_b64 vcc, -1, 0
	s_cmp_gt_i32 s72, -1
	s_cselect_b64 s[44:45], -1, 0
	s_xor_b64 s[44:45], s[0:1], s[44:45]
	v_add_u32_e32 v219, s73, v0
	s_and_b64 s[44:45], vcc, s[44:45]
	v_add_u32_e32 v220, 0x21700, v219
	s_and_b64 vcc, exec, vcc
	s_cbranch_vccnz .LBB0_214
	v_add_u32_e32 v2, 0x21780, v219
	v_add_u32_e32 v3, 0x21708, v219
	v_add_u32_e32 v4, 0x21788, v219
	ds_read2_b32 v[160:161], v220 offset1:1
	ds_read2_b32 v[144:145], v2 offset1:1
	ds_read2_b32 v[162:163], v3 offset1:1
	ds_read2_b32 v[146:147], v4 offset1:1
	v_add_u32_e32 v2, 0x21720, v219
	v_add_u32_e32 v3, 0x217a0, v219
	v_add_u32_e32 v4, 0x21728, v219
	v_add_u32_e32 v5, 0x217a8, v219
	ds_read2_b32 v[164:165], v2 offset1:1
	ds_read2_b32 v[148:149], v3 offset1:1
	ds_read2_b32 v[166:167], v4 offset1:1
	ds_read2_b32 v[150:151], v5 offset1:1
	v_add_u32_e32 v2, 0x21740, v219
	v_add_u32_e32 v3, 0x217c0, v219
	v_add_u32_e32 v4, 0x21748, v219
	v_add_u32_e32 v5, 0x217c8, v219
	ds_read2_b32 v[168:169], v2 offset1:1
	ds_read2_b32 v[152:153], v3 offset1:1
	ds_read2_b32 v[170:171], v4 offset1:1
	ds_read2_b32 v[154:155], v5 offset1:1
	v_add_u32_e32 v2, 0x21760, v219
	v_add_u32_e32 v3, 0x217e0, v219
	v_add_u32_e32 v4, 0x21768, v219
	v_add_u32_e32 v5, 0x217e8, v219
	ds_read2_b32 v[172:173], v2 offset1:1
	ds_read2_b32 v[156:157], v3 offset1:1
	ds_read2_b32 v[174:175], v4 offset1:1
	ds_read2_b32 v[158:159], v5 offset1:1
	s_branch .LBB0_215
